# speedup vs baseline: 1.0259x; 1.0259x over previous
.LBB2_8:
	s_or_b64 exec, exec, s[12:13]
	s_waitcnt vmcnt(1)
	s_mov_b32 vcc_lo, 0x55555555
	s_mov_b32 vcc_hi, 0x55555555
	s_nop 1
	v_mov_b32_dpp v142, v62 quad_perm:[0,0,1,1] row_mask:0xf bank_mask:0xf
	v_mov_b32_dpp v143, v62 quad_perm:[2,2,3,3] row_mask:0xf bank_mask:0xf
	v_mov_b32_dpp v144, v63 quad_perm:[0,0,1,1] row_mask:0xf bank_mask:0xf
	v_mov_b32_dpp v145, v63 quad_perm:[2,2,3,3] row_mask:0xf bank_mask:0xf
	v_cndmask_b32_dpp v62, v64, v142, vcc quad_perm:[0,0,1,1] row_mask:0xf bank_mask:0xf
	v_cndmask_b32_dpp v64, v64, v143, vcc quad_perm:[2,2,3,3] row_mask:0xf bank_mask:0xf
	v_cndmask_b32_dpp v63, v65, v144, vcc quad_perm:[0,0,1,1] row_mask:0xf bank_mask:0xf
	v_cndmask_b32_dpp v65, v65, v145, vcc quad_perm:[2,2,3,3] row_mask:0xf bank_mask:0xf
	v_mov_b32_dpp v142, v58 quad_perm:[0,0,1,1] row_mask:0xf bank_mask:0xf
	v_mov_b32_dpp v143, v58 quad_perm:[2,2,3,3] row_mask:0xf bank_mask:0xf
	v_mov_b32_dpp v144, v59 quad_perm:[0,0,1,1] row_mask:0xf bank_mask:0xf
	v_mov_b32_dpp v145, v59 quad_perm:[2,2,3,3] row_mask:0xf bank_mask:0xf
	v_cndmask_b32_dpp v58, v60, v142, vcc quad_perm:[0,0,1,1] row_mask:0xf bank_mask:0xf
	v_cndmask_b32_dpp v60, v60, v143, vcc quad_perm:[2,2,3,3] row_mask:0xf bank_mask:0xf
	v_cndmask_b32_dpp v59, v61, v144, vcc quad_perm:[0,0,1,1] row_mask:0xf bank_mask:0xf
	v_cndmask_b32_dpp v61, v61, v145, vcc quad_perm:[2,2,3,3] row_mask:0xf bank_mask:0xf
	v_mov_b32_dpp v142, v54 quad_perm:[0,0,1,1] row_mask:0xf bank_mask:0xf
	v_mov_b32_dpp v143, v54 quad_perm:[2,2,3,3] row_mask:0xf bank_mask:0xf
	v_mov_b32_dpp v144, v55 quad_perm:[0,0,1,1] row_mask:0xf bank_mask:0xf
	v_mov_b32_dpp v145, v55 quad_perm:[2,2,3,3] row_mask:0xf bank_mask:0xf
	v_cndmask_b32_dpp v54, v56, v142, vcc quad_perm:[0,0,1,1] row_mask:0xf bank_mask:0xf
	v_cndmask_b32_dpp v56, v56, v143, vcc quad_perm:[2,2,3,3] row_mask:0xf bank_mask:0xf
	v_cndmask_b32_dpp v55, v57, v144, vcc quad_perm:[0,0,1,1] row_mask:0xf bank_mask:0xf
	v_cndmask_b32_dpp v57, v57, v145, vcc quad_perm:[2,2,3,3] row_mask:0xf bank_mask:0xf
	v_mov_b32_dpp v142, v50 quad_perm:[0,0,1,1] row_mask:0xf bank_mask:0xf
	v_mov_b32_dpp v143, v50 quad_perm:[2,2,3,3] row_mask:0xf bank_mask:0xf
	v_mov_b32_dpp v144, v51 quad_perm:[0,0,1,1] row_mask:0xf bank_mask:0xf
	v_mov_b32_dpp v145, v51 quad_perm:[2,2,3,3] row_mask:0xf bank_mask:0xf
	v_cndmask_b32_dpp v50, v52, v142, vcc quad_perm:[0,0,1,1] row_mask:0xf bank_mask:0xf
	v_cndmask_b32_dpp v52, v52, v143, vcc quad_perm:[2,2,3,3] row_mask:0xf bank_mask:0xf
	v_cndmask_b32_dpp v51, v53, v144, vcc quad_perm:[0,0,1,1] row_mask:0xf bank_mask:0xf
	v_cndmask_b32_dpp v53, v53, v145, vcc quad_perm:[2,2,3,3] row_mask:0xf bank_mask:0xf
	v_mov_b32_dpp v142, v46 quad_perm:[0,0,1,1] row_mask:0xf bank_mask:0xf
	v_mov_b32_dpp v143, v46 quad_perm:[2,2,3,3] row_mask:0xf bank_mask:0xf
	v_mov_b32_dpp v144, v47 quad_perm:[0,0,1,1] row_mask:0xf bank_mask:0xf
	v_mov_b32_dpp v145, v47 quad_perm:[2,2,3,3] row_mask:0xf bank_mask:0xf
	v_cndmask_b32_dpp v46, v48, v142, vcc quad_perm:[0,0,1,1] row_mask:0xf bank_mask:0xf
	v_cndmask_b32_dpp v48, v48, v143, vcc quad_perm:[2,2,3,3] row_mask:0xf bank_mask:0xf
	v_cndmask_b32_dpp v47, v49, v144, vcc quad_perm:[0,0,1,1] row_mask:0xf bank_mask:0xf
	v_cndmask_b32_dpp v49, v49, v145, vcc quad_perm:[2,2,3,3] row_mask:0xf bank_mask:0xf
	v_mov_b32_dpp v142, v42 quad_perm:[0,0,1,1] row_mask:0xf bank_mask:0xf
	v_mov_b32_dpp v143, v42 quad_perm:[2,2,3,3] row_mask:0xf bank_mask:0xf
	v_mov_b32_dpp v144, v43 quad_perm:[0,0,1,1] row_mask:0xf bank_mask:0xf
	v_mov_b32_dpp v145, v43 quad_perm:[2,2,3,3] row_mask:0xf bank_mask:0xf
	v_cndmask_b32_dpp v42, v44, v142, vcc quad_perm:[0,0,1,1] row_mask:0xf bank_mask:0xf
	v_cndmask_b32_dpp v44, v44, v143, vcc quad_perm:[2,2,3,3] row_mask:0xf bank_mask:0xf
	v_cndmask_b32_dpp v43, v45, v144, vcc quad_perm:[0,0,1,1] row_mask:0xf bank_mask:0xf
	v_cndmask_b32_dpp v45, v45, v145, vcc quad_perm:[2,2,3,3] row_mask:0xf bank_mask:0xf
	v_mov_b32_dpp v142, v38 quad_perm:[0,0,1,1] row_mask:0xf bank_mask:0xf
	v_mov_b32_dpp v143, v38 quad_perm:[2,2,3,3] row_mask:0xf bank_mask:0xf
	v_mov_b32_dpp v144, v39 quad_perm:[0,0,1,1] row_mask:0xf bank_mask:0xf
	v_mov_b32_dpp v145, v39 quad_perm:[2,2,3,3] row_mask:0xf bank_mask:0xf
	v_cndmask_b32_dpp v38, v40, v142, vcc quad_perm:[0,0,1,1] row_mask:0xf bank_mask:0xf
	v_cndmask_b32_dpp v40, v40, v143, vcc quad_perm:[2,2,3,3] row_mask:0xf bank_mask:0xf
	v_cndmask_b32_dpp v39, v41, v144, vcc quad_perm:[0,0,1,1] row_mask:0xf bank_mask:0xf
	v_cndmask_b32_dpp v41, v41, v145, vcc quad_perm:[2,2,3,3] row_mask:0xf bank_mask:0xf
	v_mov_b32_dpp v142, v34 quad_perm:[0,0,1,1] row_mask:0xf bank_mask:0xf
	v_mov_b32_dpp v143, v34 quad_perm:[2,2,3,3] row_mask:0xf bank_mask:0xf
	v_mov_b32_dpp v144, v35 quad_perm:[0,0,1,1] row_mask:0xf bank_mask:0xf
	v_mov_b32_dpp v145, v35 quad_perm:[2,2,3,3] row_mask:0xf bank_mask:0xf
	v_cndmask_b32_dpp v34, v36, v142, vcc quad_perm:[0,0,1,1] row_mask:0xf bank_mask:0xf
	v_cndmask_b32_dpp v36, v36, v143, vcc quad_perm:[2,2,3,3] row_mask:0xf bank_mask:0xf
	v_cndmask_b32_dpp v35, v37, v144, vcc quad_perm:[0,0,1,1] row_mask:0xf bank_mask:0xf
	v_cndmask_b32_dpp v37, v37, v145, vcc quad_perm:[2,2,3,3] row_mask:0xf bank_mask:0xf
	v_mov_b32_dpp v142, v30 quad_perm:[0,0,1,1] row_mask:0xf bank_mask:0xf
	v_mov_b32_dpp v143, v30 quad_perm:[2,2,3,3] row_mask:0xf bank_mask:0xf
	v_mov_b32_dpp v144, v31 quad_perm:[0,0,1,1] row_mask:0xf bank_mask:0xf
	v_mov_b32_dpp v145, v31 quad_perm:[2,2,3,3] row_mask:0xf bank_mask:0xf
	v_cndmask_b32_dpp v30, v32, v142, vcc quad_perm:[0,0,1,1] row_mask:0xf bank_mask:0xf
	v_cndmask_b32_dpp v32, v32, v143, vcc quad_perm:[2,2,3,3] row_mask:0xf bank_mask:0xf
	v_cndmask_b32_dpp v31, v33, v144, vcc quad_perm:[0,0,1,1] row_mask:0xf bank_mask:0xf
	v_cndmask_b32_dpp v33, v33, v145, vcc quad_perm:[2,2,3,3] row_mask:0xf bank_mask:0xf
	v_mov_b32_dpp v142, v26 quad_perm:[0,0,1,1] row_mask:0xf bank_mask:0xf
	v_mov_b32_dpp v143, v26 quad_perm:[2,2,3,3] row_mask:0xf bank_mask:0xf
	v_mov_b32_dpp v144, v27 quad_perm:[0,0,1,1] row_mask:0xf bank_mask:0xf
	v_mov_b32_dpp v145, v27 quad_perm:[2,2,3,3] row_mask:0xf bank_mask:0xf
	v_cndmask_b32_dpp v26, v28, v142, vcc quad_perm:[0,0,1,1] row_mask:0xf bank_mask:0xf
	v_cndmask_b32_dpp v28, v28, v143, vcc quad_perm:[2,2,3,3] row_mask:0xf bank_mask:0xf
	v_cndmask_b32_dpp v27, v29, v144, vcc quad_perm:[0,0,1,1] row_mask:0xf bank_mask:0xf
	v_cndmask_b32_dpp v29, v29, v145, vcc quad_perm:[2,2,3,3] row_mask:0xf bank_mask:0xf
	v_mov_b32_dpp v142, v22 quad_perm:[0,0,1,1] row_mask:0xf bank_mask:0xf
	v_mov_b32_dpp v143, v22 quad_perm:[2,2,3,3] row_mask:0xf bank_mask:0xf
	v_mov_b32_dpp v144, v23 quad_perm:[0,0,1,1] row_mask:0xf bank_mask:0xf
	v_mov_b32_dpp v145, v23 quad_perm:[2,2,3,3] row_mask:0xf bank_mask:0xf
	v_cndmask_b32_dpp v22, v24, v142, vcc quad_perm:[0,0,1,1] row_mask:0xf bank_mask:0xf
	v_cndmask_b32_dpp v24, v24, v143, vcc quad_perm:[2,2,3,3] row_mask:0xf bank_mask:0xf
	v_cndmask_b32_dpp v23, v25, v144, vcc quad_perm:[0,0,1,1] row_mask:0xf bank_mask:0xf
	v_cndmask_b32_dpp v25, v25, v145, vcc quad_perm:[2,2,3,3] row_mask:0xf bank_mask:0xf
	v_cvt_f32_f16_e32 v124, v62
	v_cvt_f32_f16_sdwa v126, v62 dst_sel:DWORD dst_unused:UNUSED_PAD src0_sel:WORD_1
	v_cvt_f32_f16_e32 v132, v63
	v_cvt_f32_f16_sdwa v133, v63 dst_sel:DWORD dst_unused:UNUSED_PAD src0_sel:WORD_1
	v_cvt_f32_f16_e32 v129, v64
	v_cvt_f32_f16_sdwa v131, v64 dst_sel:DWORD dst_unused:UNUSED_PAD src0_sel:WORD_1
	v_cvt_f32_f16_e32 v134, v65
	v_cvt_f32_f16_sdwa v135, v65 dst_sel:DWORD dst_unused:UNUSED_PAD src0_sel:WORD_1
	s_mov_b32 s12, 0xff7fffff
	v_cvt_f32_f16_e32 v117, v58
	v_cvt_f32_f16_sdwa v120, v58 dst_sel:DWORD dst_unused:UNUSED_PAD src0_sel:WORD_1
	v_cvt_f32_f16_e32 v121, v60
	v_cvt_f32_f16_sdwa v123, v60 dst_sel:DWORD dst_unused:UNUSED_PAD src0_sel:WORD_1
	v_cvt_f32_f16_e32 v109, v54
	v_cvt_f32_f16_sdwa v112, v54 dst_sel:DWORD dst_unused:UNUSED_PAD src0_sel:WORD_1
	v_cvt_f32_f16_e32 v116, v55
	v_cvt_f32_f16_sdwa v118, v55 dst_sel:DWORD dst_unused:UNUSED_PAD src0_sel:WORD_1
	v_cvt_f32_f16_e32 v113, v56
	v_cvt_f32_f16_sdwa v115, v56 dst_sel:DWORD dst_unused:UNUSED_PAD src0_sel:WORD_1
	v_cvt_f32_f16_e32 v119, v57
	v_cvt_f32_f16_sdwa v122, v57 dst_sel:DWORD dst_unused:UNUSED_PAD src0_sel:WORD_1
	v_cvt_f32_f16_e32 v101, v50
	v_cvt_f32_f16_sdwa v104, v50 dst_sel:DWORD dst_unused:UNUSED_PAD src0_sel:WORD_1
	v_cvt_f32_f16_e32 v108, v51
	v_cvt_f32_f16_sdwa v110, v51 dst_sel:DWORD dst_unused:UNUSED_PAD src0_sel:WORD_1
	v_cvt_f32_f16_e32 v105, v52
	v_cvt_f32_f16_sdwa v107, v52 dst_sel:DWORD dst_unused:UNUSED_PAD src0_sel:WORD_1
	v_cvt_f32_f16_e32 v111, v53
	v_cvt_f32_f16_sdwa v114, v53 dst_sel:DWORD dst_unused:UNUSED_PAD src0_sel:WORD_1
	v_cvt_f32_f16_e32 v93, v46
	v_cvt_f32_f16_sdwa v96, v46 dst_sel:DWORD dst_unused:UNUSED_PAD src0_sel:WORD_1
	v_cvt_f32_f16_e32 v100, v47
	v_cvt_f32_f16_sdwa v102, v47 dst_sel:DWORD dst_unused:UNUSED_PAD src0_sel:WORD_1
	v_cvt_f32_f16_e32 v97, v48
	v_cvt_f32_f16_sdwa v99, v48 dst_sel:DWORD dst_unused:UNUSED_PAD src0_sel:WORD_1
	v_cvt_f32_f16_e32 v103, v49
	v_cvt_f32_f16_sdwa v106, v49 dst_sel:DWORD dst_unused:UNUSED_PAD src0_sel:WORD_1
	v_cvt_f32_f16_e32 v85, v42
	v_cvt_f32_f16_sdwa v88, v42 dst_sel:DWORD dst_unused:UNUSED_PAD src0_sel:WORD_1
	v_cvt_f32_f16_e32 v92, v43
	v_cvt_f32_f16_sdwa v94, v43 dst_sel:DWORD dst_unused:UNUSED_PAD src0_sel:WORD_1
	v_cvt_f32_f16_e32 v89, v44
	v_cvt_f32_f16_sdwa v91, v44 dst_sel:DWORD dst_unused:UNUSED_PAD src0_sel:WORD_1
	v_cvt_f32_f16_e32 v95, v45
	v_cvt_f32_f16_sdwa v98, v45 dst_sel:DWORD dst_unused:UNUSED_PAD src0_sel:WORD_1
	v_cvt_f32_f16_e32 v63, v38
	v_cvt_f32_f16_sdwa v72, v38 dst_sel:DWORD dst_unused:UNUSED_PAD src0_sel:WORD_1
	v_cvt_f32_f16_e32 v80, v39
	v_cvt_f32_f16_sdwa v86, v39 dst_sel:DWORD dst_unused:UNUSED_PAD src0_sel:WORD_1
	v_cvt_f32_f16_e32 v73, v40
	v_cvt_f32_f16_sdwa v79, v40 dst_sel:DWORD dst_unused:UNUSED_PAD src0_sel:WORD_1
	v_cvt_f32_f16_e32 v87, v41
	v_cvt_f32_f16_sdwa v90, v41 dst_sel:DWORD dst_unused:UNUSED_PAD src0_sel:WORD_1
	v_cvt_f32_f16_e32 v51, v34
	v_cvt_f32_f16_sdwa v54, v34 dst_sel:DWORD dst_unused:UNUSED_PAD src0_sel:WORD_1
	v_cvt_f32_f16_e32 v60, v35
	v_cvt_f32_f16_sdwa v64, v35 dst_sel:DWORD dst_unused:UNUSED_PAD src0_sel:WORD_1
	v_cvt_f32_f16_e32 v55, v36
	v_cvt_f32_f16_sdwa v57, v36 dst_sel:DWORD dst_unused:UNUSED_PAD src0_sel:WORD_1
	v_cvt_f32_f16_e32 v65, v37
	v_cvt_f32_f16_sdwa v74, v37 dst_sel:DWORD dst_unused:UNUSED_PAD src0_sel:WORD_1
	v_cvt_f32_f16_e32 v43, v30
	v_cvt_f32_f16_sdwa v46, v30 dst_sel:DWORD dst_unused:UNUSED_PAD src0_sel:WORD_1
	v_cvt_f32_f16_e32 v50, v31
	v_cvt_f32_f16_sdwa v52, v31 dst_sel:DWORD dst_unused:UNUSED_PAD src0_sel:WORD_1
	v_cvt_f32_f16_e32 v47, v32
	v_cvt_f32_f16_sdwa v49, v32 dst_sel:DWORD dst_unused:UNUSED_PAD src0_sel:WORD_1
	v_cvt_f32_f16_e32 v53, v33
	v_cvt_f32_f16_sdwa v56, v33 dst_sel:DWORD dst_unused:UNUSED_PAD src0_sel:WORD_1
	v_cvt_f32_f16_e32 v35, v26
	v_cvt_f32_f16_sdwa v38, v26 dst_sel:DWORD dst_unused:UNUSED_PAD src0_sel:WORD_1
	v_cvt_f32_f16_e32 v42, v27
	v_cvt_f32_f16_sdwa v44, v27 dst_sel:DWORD dst_unused:UNUSED_PAD src0_sel:WORD_1
	v_cvt_f32_f16_e32 v39, v28
	v_cvt_f32_f16_sdwa v41, v28 dst_sel:DWORD dst_unused:UNUSED_PAD src0_sel:WORD_1
	v_cvt_f32_f16_e32 v45, v29
	v_cvt_f32_f16_sdwa v48, v29 dst_sel:DWORD dst_unused:UNUSED_PAD src0_sel:WORD_1
	v_cvt_f32_f16_e32 v27, v22
	v_cvt_f32_f16_sdwa v30, v22 dst_sel:DWORD dst_unused:UNUSED_PAD src0_sel:WORD_1
	v_cvt_f32_f16_e32 v34, v23
	v_cvt_f32_f16_sdwa v36, v23 dst_sel:DWORD dst_unused:UNUSED_PAD src0_sel:WORD_1
	v_cvt_f32_f16_e32 v31, v24
	v_cvt_f32_f16_sdwa v33, v24 dst_sel:DWORD dst_unused:UNUSED_PAD src0_sel:WORD_1
	v_cvt_f32_f16_e32 v37, v25
	v_cvt_f32_f16_sdwa v40, v25 dst_sel:DWORD dst_unused:UNUSED_PAD src0_sel:WORD_1
	s_waitcnt vmcnt(0)
	s_mov_b32 vcc_lo, 0x55555555
	s_mov_b32 vcc_hi, 0x55555555
	s_nop 1
	v_mov_b32_dpp v142, v18 quad_perm:[0,0,1,1] row_mask:0xf bank_mask:0xf
	v_mov_b32_dpp v143, v18 quad_perm:[2,2,3,3] row_mask:0xf bank_mask:0xf
	v_mov_b32_dpp v144, v19 quad_perm:[0,0,1,1] row_mask:0xf bank_mask:0xf
	v_mov_b32_dpp v145, v19 quad_perm:[2,2,3,3] row_mask:0xf bank_mask:0xf
	v_cndmask_b32_dpp v18, v20, v142, vcc quad_perm:[0,0,1,1] row_mask:0xf bank_mask:0xf
	v_cndmask_b32_dpp v20, v20, v143, vcc quad_perm:[2,2,3,3] row_mask:0xf bank_mask:0xf
	v_cndmask_b32_dpp v19, v21, v144, vcc quad_perm:[0,0,1,1] row_mask:0xf bank_mask:0xf
	v_cndmask_b32_dpp v21, v21, v145, vcc quad_perm:[2,2,3,3] row_mask:0xf bank_mask:0xf
	v_mov_b32_dpp v142, v14 quad_perm:[0,0,1,1] row_mask:0xf bank_mask:0xf
	v_mov_b32_dpp v143, v14 quad_perm:[2,2,3,3] row_mask:0xf bank_mask:0xf
	v_mov_b32_dpp v144, v15 quad_perm:[0,0,1,1] row_mask:0xf bank_mask:0xf
	v_mov_b32_dpp v145, v15 quad_perm:[2,2,3,3] row_mask:0xf bank_mask:0xf
	v_cndmask_b32_dpp v14, v16, v142, vcc quad_perm:[0,0,1,1] row_mask:0xf bank_mask:0xf
	v_cndmask_b32_dpp v16, v16, v143, vcc quad_perm:[2,2,3,3] row_mask:0xf bank_mask:0xf
	v_cndmask_b32_dpp v15, v17, v144, vcc quad_perm:[0,0,1,1] row_mask:0xf bank_mask:0xf
	v_cndmask_b32_dpp v17, v17, v145, vcc quad_perm:[2,2,3,3] row_mask:0xf bank_mask:0xf
	v_mov_b32_dpp v142, v6 quad_perm:[0,0,1,1] row_mask:0xf bank_mask:0xf
	v_mov_b32_dpp v143, v6 quad_perm:[2,2,3,3] row_mask:0xf bank_mask:0xf
	v_mov_b32_dpp v144, v7 quad_perm:[0,0,1,1] row_mask:0xf bank_mask:0xf
	v_mov_b32_dpp v145, v7 quad_perm:[2,2,3,3] row_mask:0xf bank_mask:0xf
	v_cndmask_b32_dpp v6, v8, v142, vcc quad_perm:[0,0,1,1] row_mask:0xf bank_mask:0xf
	v_cndmask_b32_dpp v8, v8, v143, vcc quad_perm:[2,2,3,3] row_mask:0xf bank_mask:0xf
	v_cndmask_b32_dpp v7, v9, v144, vcc quad_perm:[0,0,1,1] row_mask:0xf bank_mask:0xf
	v_cndmask_b32_dpp v9, v9, v145, vcc quad_perm:[2,2,3,3] row_mask:0xf bank_mask:0xf
	v_mov_b32_dpp v142, v10 quad_perm:[0,0,1,1] row_mask:0xf bank_mask:0xf
	v_mov_b32_dpp v143, v10 quad_perm:[2,2,3,3] row_mask:0xf bank_mask:0xf
	v_mov_b32_dpp v144, v11 quad_perm:[0,0,1,1] row_mask:0xf bank_mask:0xf
	v_mov_b32_dpp v145, v11 quad_perm:[2,2,3,3] row_mask:0xf bank_mask:0xf
	v_cndmask_b32_dpp v10, v12, v142, vcc quad_perm:[0,0,1,1] row_mask:0xf bank_mask:0xf
	v_cndmask_b32_dpp v12, v12, v143, vcc quad_perm:[2,2,3,3] row_mask:0xf bank_mask:0xf
	v_cndmask_b32_dpp v11, v13, v144, vcc quad_perm:[0,0,1,1] row_mask:0xf bank_mask:0xf
	v_cndmask_b32_dpp v13, v13, v145, vcc quad_perm:[2,2,3,3] row_mask:0xf bank_mask:0xf
	v_mov_b32_dpp v142, v2 quad_perm:[0,0,1,1] row_mask:0xf bank_mask:0xf
	v_mov_b32_dpp v143, v2 quad_perm:[2,2,3,3] row_mask:0xf bank_mask:0xf
	v_mov_b32_dpp v144, v3 quad_perm:[0,0,1,1] row_mask:0xf bank_mask:0xf
	v_mov_b32_dpp v145, v3 quad_perm:[2,2,3,3] row_mask:0xf bank_mask:0xf
	v_cndmask_b32_dpp v2, v4, v142, vcc quad_perm:[0,0,1,1] row_mask:0xf bank_mask:0xf
	v_cndmask_b32_dpp v4, v4, v143, vcc quad_perm:[2,2,3,3] row_mask:0xf bank_mask:0xf
	v_cndmask_b32_dpp v3, v5, v144, vcc quad_perm:[0,0,1,1] row_mask:0xf bank_mask:0xf
	v_cndmask_b32_dpp v5, v5, v145, vcc quad_perm:[2,2,3,3] row_mask:0xf bank_mask:0xf
	v_mov_b32_e32 v67, v6
	v_cvt_f32_f16_e32 v22, v18
	v_cvt_f32_f16_sdwa v23, v18 dst_sel:DWORD dst_unused:UNUSED_PAD src0_sel:WORD_1
	v_cvt_f32_f16_e32 v26, v19
	v_cvt_f32_f16_sdwa v28, v19 dst_sel:DWORD dst_unused:UNUSED_PAD src0_sel:WORD_1
	v_cvt_f32_f16_e32 v24, v20
	v_cvt_f32_f16_sdwa v25, v20 dst_sel:DWORD dst_unused:UNUSED_PAD src0_sel:WORD_1
	v_cvt_f32_f16_e32 v29, v21
	v_cvt_f32_f16_sdwa v32, v21 dst_sel:DWORD dst_unused:UNUSED_PAD src0_sel:WORD_1
	v_cvt_f32_f16_e32 v18, v14
	v_cvt_f32_f16_sdwa v6, v14 dst_sel:DWORD dst_unused:UNUSED_PAD src0_sel:WORD_1
	v_cvt_f32_f16_e32 v20, v15
	v_cvt_f32_f16_sdwa v19, v15 dst_sel:DWORD dst_unused:UNUSED_PAD src0_sel:WORD_1
	v_cvt_f32_f16_e32 v15, v16
	v_cvt_f32_f16_sdwa v14, v16 dst_sel:DWORD dst_unused:UNUSED_PAD src0_sel:WORD_1
	v_cvt_f32_f16_e32 v21, v17
	v_cvt_f32_f16_sdwa v16, v17 dst_sel:DWORD dst_unused:UNUSED_PAD src0_sel:WORD_1
	v_max3_f32 v17, v124, s12, v126
	v_cvt_f32_f16_e32 v125, v59
	v_cvt_f32_f16_sdwa v127, v59 dst_sel:DWORD dst_unused:UNUSED_PAD src0_sel:WORD_1
	v_max3_f32 v17, v17, v132, v133
	v_max3_f32 v17, v17, v129, v131
	v_cvt_f32_f16_e32 v128, v61
	v_cvt_f32_f16_sdwa v130, v61 dst_sel:DWORD dst_unused:UNUSED_PAD src0_sel:WORD_1
	v_max3_f32 v17, v17, v134, v135
	v_max3_f32 v17, v17, v117, v120
	v_max3_f32 v17, v17, v125, v127
	v_max3_f32 v17, v17, v121, v123
	v_max3_f32 v17, v17, v128, v130
	v_max3_f32 v17, v17, v109, v112
	v_max3_f32 v17, v17, v116, v118
	v_max3_f32 v17, v17, v113, v115
	v_max3_f32 v17, v17, v119, v122
	v_max3_f32 v17, v17, v101, v104
	v_max3_f32 v17, v17, v108, v110
	v_max3_f32 v17, v17, v105, v107
	v_max3_f32 v17, v17, v111, v114
	v_max3_f32 v17, v17, v93, v96
	v_max3_f32 v17, v17, v100, v102
	v_max3_f32 v17, v17, v97, v99
	v_max3_f32 v17, v17, v103, v106
	v_max3_f32 v17, v17, v85, v88
	v_max3_f32 v17, v17, v92, v94
	v_max3_f32 v17, v17, v89, v91
	v_max3_f32 v17, v17, v95, v98
	v_max3_f32 v17, v17, v63, v72
	v_max3_f32 v17, v17, v80, v86
	v_max3_f32 v17, v17, v73, v79
	v_max3_f32 v17, v17, v87, v90
	v_max3_f32 v17, v17, v51, v54
	v_max3_f32 v17, v17, v60, v64
	v_max3_f32 v17, v17, v55, v57
	v_max3_f32 v17, v17, v65, v74
	v_max3_f32 v17, v17, v43, v46
	v_max3_f32 v17, v17, v50, v52
	v_max3_f32 v17, v17, v47, v49
	v_max3_f32 v17, v17, v53, v56
	v_max3_f32 v17, v17, v35, v38
	v_max3_f32 v17, v17, v42, v44
	v_max3_f32 v17, v17, v39, v41
	v_max3_f32 v17, v17, v45, v48
	v_max3_f32 v17, v17, v27, v30
	v_max3_f32 v17, v17, v34, v36
	v_max3_f32 v17, v17, v31, v33
	v_max3_f32 v17, v17, v37, v40
	v_max3_f32 v17, v17, v22, v23
	v_max3_f32 v17, v17, v26, v28
	v_max3_f32 v17, v17, v24, v25
	s_movk_i32 s12, 0x3a0
	v_max3_f32 v136, v17, v29, v32
	v_cmp_gt_u32_e32 vcc, s12, v0
	s_and_saveexec_b64 s[12:13], vcc
	v_max3_f32 v17, v136, v18, v6
	v_max3_f32 v17, v17, v20, v19
	v_max3_f32 v17, v17, v15, v14
	v_max3_f32 v136, v17, v21, v16
	s_or_b64 exec, exec, s[12:13]
	v_cvt_f32_f16_e32 v77, v67
	v_cvt_f32_f16_sdwa v75, v67 dst_sel:DWORD dst_unused:UNUSED_PAD src0_sel:WORD_1
	v_cvt_f32_f16_e32 v83, v7
	v_cvt_f32_f16_sdwa v81, v7 dst_sel:DWORD dst_unused:UNUSED_PAD src0_sel:WORD_1
	v_cvt_f32_f16_e32 v78, v8
	v_cvt_f32_f16_sdwa v76, v8 dst_sel:DWORD dst_unused:UNUSED_PAD src0_sel:WORD_1
	v_cvt_f32_f16_e32 v84, v9
	v_cvt_f32_f16_sdwa v82, v9 dst_sel:DWORD dst_unused:UNUSED_PAD src0_sel:WORD_1
	s_and_saveexec_b64 s[12:13], s[2:3]
	v_max3_f32 v7, v136, v77, v75
	v_max3_f32 v7, v7, v83, v81
	v_max3_f32 v7, v7, v78, v76
	v_max3_f32 v136, v7, v84, v82
	s_or_b64 exec, exec, s[12:13]
	v_cvt_f32_f16_e32 v61, v10
	v_cvt_f32_f16_sdwa v58, v10 dst_sel:DWORD dst_unused:UNUSED_PAD src0_sel:WORD_1
	v_cvt_f32_f16_e32 v68, v11
	v_cvt_f32_f16_sdwa v66, v11 dst_sel:DWORD dst_unused:UNUSED_PAD src0_sel:WORD_1
	v_cvt_f32_f16_e32 v62, v12
	v_cvt_f32_f16_sdwa v59, v12 dst_sel:DWORD dst_unused:UNUSED_PAD src0_sel:WORD_1
	v_cvt_f32_f16_e32 v69, v13
	v_cvt_f32_f16_sdwa v67, v13 dst_sel:DWORD dst_unused:UNUSED_PAD src0_sel:WORD_1
	s_and_saveexec_b64 s[12:13], s[4:5]
	v_max3_f32 v7, v136, v61, v58
	v_max3_f32 v7, v7, v68, v66
	v_max3_f32 v7, v7, v62, v59
	v_max3_f32 v136, v7, v69, v67
	s_or_b64 exec, exec, s[12:13]
	v_cvt_f32_f16_e32 v9, v2
	v_cvt_f32_f16_sdwa v7, v2 dst_sel:DWORD dst_unused:UNUSED_PAD src0_sel:WORD_1
	v_cvt_f32_f16_e32 v13, v3
	v_cvt_f32_f16_sdwa v11, v3 dst_sel:DWORD dst_unused:UNUSED_PAD src0_sel:WORD_1
	v_cvt_f32_f16_e32 v10, v4
	v_cvt_f32_f16_sdwa v8, v4 dst_sel:DWORD dst_unused:UNUSED_PAD src0_sel:WORD_1
	v_cvt_f32_f16_e32 v17, v5
	v_cvt_f32_f16_sdwa v12, v5 dst_sel:DWORD dst_unused:UNUSED_PAD src0_sel:WORD_1
	s_and_saveexec_b64 s[12:13], s[6:7]
	v_max3_f32 v2, v136, v9, v7
	v_max3_f32 v2, v2, v13, v11
	v_max3_f32 v2, v2, v10, v8
	v_max3_f32 v136, v2, v17, v12
	s_or_b64 exec, exec, s[12:13]
	v_sub_f32_e32 v2, v124, v136
	v_mul_f32_e32 v2, 0x3fb8aa3b, v2
	v_sub_f32_e32 v3, v126, v136
	v_exp_f32_e32 v2, v2
	v_mul_f32_e32 v3, 0x3fb8aa3b, v3
	v_sub_f32_e32 v4, v132, v136
	v_exp_f32_e32 v3, v3
	v_mul_f32_e32 v4, 0x3fb8aa3b, v4
	v_sub_f32_e32 v5, v133, v136
	v_exp_f32_e32 v4, v4
	v_mul_f32_e32 v5, 0x3fb8aa3b, v5
	v_exp_f32_e32 v5, v5
	v_add_f32_e32 v2, 0, v2
	v_add_f32_e32 v2, v2, v3
	v_sub_f32_e32 v3, v129, v136
	v_add_f32_e32 v2, v2, v4
	v_mul_f32_e32 v3, 0x3fb8aa3b, v3
	v_sub_f32_e32 v4, v131, v136
	v_add_f32_e32 v2, v2, v5
	v_exp_f32_e32 v3, v3
	v_mul_f32_e32 v4, 0x3fb8aa3b, v4
	v_sub_f32_e32 v5, v134, v136
	v_exp_f32_e32 v4, v4
	v_mul_f32_e32 v5, 0x3fb8aa3b, v5
	v_sub_f32_e32 v137, v135, v136
	v_exp_f32_e32 v5, v5
	v_mul_f32_e32 v137, 0x3fb8aa3b, v137
	v_exp_f32_e32 v137, v137
	v_add_f32_e32 v2, v2, v3
	v_sub_f32_e32 v3, v117, v136
	v_add_f32_e32 v2, v2, v4
	v_mul_f32_e32 v3, 0x3fb8aa3b, v3
	v_sub_f32_e32 v4, v120, v136
	v_add_f32_e32 v2, v2, v5
	v_exp_f32_e32 v3, v3
	v_mul_f32_e32 v4, 0x3fb8aa3b, v4
	v_sub_f32_e32 v5, v125, v136
	v_add_f32_e32 v2, v2, v137
	v_exp_f32_e32 v4, v4
	v_mul_f32_e32 v5, 0x3fb8aa3b, v5
	v_sub_f32_e32 v137, v127, v136
	v_exp_f32_e32 v5, v5
	v_mul_f32_e32 v137, 0x3fb8aa3b, v137
	v_exp_f32_e32 v137, v137
	v_add_f32_e32 v2, v2, v3
	v_sub_f32_e32 v3, v121, v136
	v_add_f32_e32 v2, v2, v4
	v_mul_f32_e32 v3, 0x3fb8aa3b, v3
	v_sub_f32_e32 v4, v123, v136
	v_add_f32_e32 v2, v2, v5
	v_exp_f32_e32 v3, v3
	v_mul_f32_e32 v4, 0x3fb8aa3b, v4
	v_sub_f32_e32 v5, v128, v136
	v_add_f32_e32 v2, v2, v137
	v_exp_f32_e32 v4, v4
	v_mul_f32_e32 v5, 0x3fb8aa3b, v5
	v_sub_f32_e32 v137, v130, v136
	v_exp_f32_e32 v5, v5
	v_mul_f32_e32 v137, 0x3fb8aa3b, v137
	v_exp_f32_e32 v137, v137
	v_add_f32_e32 v2, v2, v3
	v_sub_f32_e32 v3, v109, v136
	v_add_f32_e32 v2, v2, v4
	v_mul_f32_e32 v3, 0x3fb8aa3b, v3
	v_sub_f32_e32 v4, v112, v136
	v_add_f32_e32 v2, v2, v5
	v_exp_f32_e32 v3, v3
	v_mul_f32_e32 v4, 0x3fb8aa3b, v4
	v_sub_f32_e32 v5, v116, v136
	v_add_f32_e32 v2, v2, v137
	v_exp_f32_e32 v4, v4
	v_mul_f32_e32 v5, 0x3fb8aa3b, v5
	v_sub_f32_e32 v137, v118, v136
	v_exp_f32_e32 v5, v5
	v_mul_f32_e32 v137, 0x3fb8aa3b, v137
	v_exp_f32_e32 v137, v137
	v_add_f32_e32 v2, v2, v3
	v_sub_f32_e32 v3, v113, v136
	v_add_f32_e32 v2, v2, v4
	v_mul_f32_e32 v3, 0x3fb8aa3b, v3
	v_sub_f32_e32 v4, v115, v136
	v_add_f32_e32 v2, v2, v5
	v_exp_f32_e32 v3, v3
	v_mul_f32_e32 v4, 0x3fb8aa3b, v4
	v_sub_f32_e32 v5, v119, v136
	v_add_f32_e32 v2, v2, v137
	v_exp_f32_e32 v4, v4
	v_mul_f32_e32 v5, 0x3fb8aa3b, v5
	v_sub_f32_e32 v137, v122, v136
	v_exp_f32_e32 v5, v5
	v_mul_f32_e32 v137, 0x3fb8aa3b, v137
	v_exp_f32_e32 v137, v137
	v_add_f32_e32 v2, v2, v3
	v_sub_f32_e32 v3, v101, v136
	v_add_f32_e32 v2, v2, v4
	v_mul_f32_e32 v3, 0x3fb8aa3b, v3
	v_sub_f32_e32 v4, v104, v136
	v_add_f32_e32 v2, v2, v5
	v_exp_f32_e32 v3, v3
	v_mul_f32_e32 v4, 0x3fb8aa3b, v4
	v_sub_f32_e32 v5, v108, v136
	v_add_f32_e32 v2, v2, v137
	v_exp_f32_e32 v4, v4
	v_mul_f32_e32 v5, 0x3fb8aa3b, v5
	v_sub_f32_e32 v137, v110, v136
	v_exp_f32_e32 v5, v5
	v_mul_f32_e32 v137, 0x3fb8aa3b, v137
	v_exp_f32_e32 v137, v137
	v_add_f32_e32 v2, v2, v3
	v_sub_f32_e32 v3, v105, v136
	v_add_f32_e32 v2, v2, v4
	v_mul_f32_e32 v3, 0x3fb8aa3b, v3
	v_sub_f32_e32 v4, v107, v136
	v_add_f32_e32 v2, v2, v5
	v_exp_f32_e32 v3, v3
	v_mul_f32_e32 v4, 0x3fb8aa3b, v4
	v_sub_f32_e32 v5, v111, v136
	v_add_f32_e32 v2, v2, v137
	v_exp_f32_e32 v4, v4
	v_mul_f32_e32 v5, 0x3fb8aa3b, v5
	v_sub_f32_e32 v137, v114, v136
	v_exp_f32_e32 v5, v5
	v_mul_f32_e32 v137, 0x3fb8aa3b, v137
	v_exp_f32_e32 v137, v137
	v_add_f32_e32 v2, v2, v3
	v_sub_f32_e32 v3, v93, v136
	v_add_f32_e32 v2, v2, v4
	v_mul_f32_e32 v3, 0x3fb8aa3b, v3
	v_sub_f32_e32 v4, v96, v136
	v_add_f32_e32 v2, v2, v5
	v_exp_f32_e32 v3, v3
	v_mul_f32_e32 v4, 0x3fb8aa3b, v4
	v_sub_f32_e32 v5, v100, v136
	v_add_f32_e32 v2, v2, v137
	v_exp_f32_e32 v4, v4
	v_mul_f32_e32 v5, 0x3fb8aa3b, v5
	v_sub_f32_e32 v137, v102, v136
	v_exp_f32_e32 v5, v5
	v_mul_f32_e32 v137, 0x3fb8aa3b, v137
	v_exp_f32_e32 v137, v137
	v_add_f32_e32 v2, v2, v3
	v_sub_f32_e32 v3, v97, v136
	v_add_f32_e32 v2, v2, v4
	v_mul_f32_e32 v3, 0x3fb8aa3b, v3
	v_sub_f32_e32 v4, v99, v136
	v_add_f32_e32 v2, v2, v5
	v_exp_f32_e32 v3, v3
	v_mul_f32_e32 v4, 0x3fb8aa3b, v4
	v_sub_f32_e32 v5, v103, v136
	v_add_f32_e32 v2, v2, v137
	v_exp_f32_e32 v4, v4
	v_mul_f32_e32 v5, 0x3fb8aa3b, v5
	v_sub_f32_e32 v137, v106, v136
	v_exp_f32_e32 v5, v5
	v_mul_f32_e32 v137, 0x3fb8aa3b, v137
	v_exp_f32_e32 v137, v137
	v_add_f32_e32 v2, v2, v3
	v_sub_f32_e32 v3, v85, v136
	v_add_f32_e32 v2, v2, v4
	v_mul_f32_e32 v3, 0x3fb8aa3b, v3
	v_sub_f32_e32 v4, v88, v136
	v_add_f32_e32 v2, v2, v5
	v_exp_f32_e32 v3, v3
	v_mul_f32_e32 v4, 0x3fb8aa3b, v4
	v_sub_f32_e32 v5, v92, v136
	v_add_f32_e32 v2, v2, v137
	v_exp_f32_e32 v4, v4
	v_mul_f32_e32 v5, 0x3fb8aa3b, v5
	v_sub_f32_e32 v137, v94, v136
	v_exp_f32_e32 v5, v5
	v_mul_f32_e32 v137, 0x3fb8aa3b, v137
	v_exp_f32_e32 v137, v137
	v_add_f32_e32 v2, v2, v3
	v_sub_f32_e32 v3, v89, v136
	v_add_f32_e32 v2, v2, v4
	v_mul_f32_e32 v3, 0x3fb8aa3b, v3
	v_sub_f32_e32 v4, v91, v136
	v_add_f32_e32 v2, v2, v5
	v_exp_f32_e32 v3, v3
	v_mul_f32_e32 v4, 0x3fb8aa3b, v4
	v_sub_f32_e32 v5, v95, v136
	v_add_f32_e32 v2, v2, v137
	v_exp_f32_e32 v4, v4
	v_mul_f32_e32 v5, 0x3fb8aa3b, v5
	v_sub_f32_e32 v137, v98, v136
	v_exp_f32_e32 v5, v5
	v_mul_f32_e32 v137, 0x3fb8aa3b, v137
	v_exp_f32_e32 v137, v137
	v_add_f32_e32 v2, v2, v3
	v_sub_f32_e32 v3, v63, v136
	v_add_f32_e32 v2, v2, v4
	v_mul_f32_e32 v3, 0x3fb8aa3b, v3
	v_sub_f32_e32 v4, v72, v136
	v_add_f32_e32 v2, v2, v5
	v_exp_f32_e32 v3, v3
	v_mul_f32_e32 v4, 0x3fb8aa3b, v4
	v_sub_f32_e32 v5, v80, v136
	v_add_f32_e32 v2, v2, v137
	v_exp_f32_e32 v4, v4
	v_mul_f32_e32 v5, 0x3fb8aa3b, v5
	v_sub_f32_e32 v137, v86, v136
	v_exp_f32_e32 v5, v5
	v_mul_f32_e32 v137, 0x3fb8aa3b, v137
	v_exp_f32_e32 v137, v137
	v_add_f32_e32 v2, v2, v3
	v_sub_f32_e32 v3, v73, v136
	v_add_f32_e32 v2, v2, v4
	v_mul_f32_e32 v3, 0x3fb8aa3b, v3
	v_sub_f32_e32 v4, v79, v136
	v_add_f32_e32 v2, v2, v5
	v_exp_f32_e32 v3, v3
	v_mul_f32_e32 v4, 0x3fb8aa3b, v4
	v_sub_f32_e32 v5, v87, v136
	v_add_f32_e32 v2, v2, v137
	v_exp_f32_e32 v4, v4
	v_mul_f32_e32 v5, 0x3fb8aa3b, v5
	v_sub_f32_e32 v137, v90, v136
	v_exp_f32_e32 v5, v5
	v_mul_f32_e32 v137, 0x3fb8aa3b, v137
	v_exp_f32_e32 v137, v137
	v_add_f32_e32 v2, v2, v3
	v_sub_f32_e32 v3, v51, v136
	v_add_f32_e32 v2, v2, v4
	v_mul_f32_e32 v3, 0x3fb8aa3b, v3
	v_sub_f32_e32 v4, v54, v136
	v_add_f32_e32 v2, v2, v5
	v_exp_f32_e32 v3, v3
	v_mul_f32_e32 v4, 0x3fb8aa3b, v4
	v_sub_f32_e32 v5, v60, v136
	v_add_f32_e32 v2, v2, v137
	v_exp_f32_e32 v4, v4
	v_mul_f32_e32 v5, 0x3fb8aa3b, v5
	v_sub_f32_e32 v137, v64, v136
	v_exp_f32_e32 v5, v5
	v_mul_f32_e32 v137, 0x3fb8aa3b, v137
	v_exp_f32_e32 v137, v137
	v_add_f32_e32 v2, v2, v3
	v_sub_f32_e32 v3, v55, v136
	v_add_f32_e32 v2, v2, v4
	v_mul_f32_e32 v3, 0x3fb8aa3b, v3
	v_sub_f32_e32 v4, v57, v136
	v_add_f32_e32 v2, v2, v5
	v_exp_f32_e32 v3, v3
	v_mul_f32_e32 v4, 0x3fb8aa3b, v4
	v_sub_f32_e32 v5, v65, v136
	v_add_f32_e32 v2, v2, v137
	v_exp_f32_e32 v4, v4
	v_mul_f32_e32 v5, 0x3fb8aa3b, v5
	v_sub_f32_e32 v137, v74, v136
	v_exp_f32_e32 v5, v5
	v_mul_f32_e32 v137, 0x3fb8aa3b, v137
	v_exp_f32_e32 v137, v137
	v_add_f32_e32 v2, v2, v3
	v_sub_f32_e32 v3, v43, v136
	v_add_f32_e32 v2, v2, v4
	v_mul_f32_e32 v3, 0x3fb8aa3b, v3
	v_sub_f32_e32 v4, v46, v136
	v_add_f32_e32 v2, v2, v5
	v_exp_f32_e32 v3, v3
	v_mul_f32_e32 v4, 0x3fb8aa3b, v4
	v_sub_f32_e32 v5, v50, v136
	v_add_f32_e32 v2, v2, v137
	v_exp_f32_e32 v4, v4
	v_mul_f32_e32 v5, 0x3fb8aa3b, v5
	v_sub_f32_e32 v137, v52, v136
	v_exp_f32_e32 v5, v5
	v_mul_f32_e32 v137, 0x3fb8aa3b, v137
	v_exp_f32_e32 v137, v137
	v_add_f32_e32 v2, v2, v3
	v_sub_f32_e32 v3, v47, v136
	v_add_f32_e32 v2, v2, v4
	v_mul_f32_e32 v3, 0x3fb8aa3b, v3
	v_sub_f32_e32 v4, v49, v136
	v_add_f32_e32 v2, v2, v5
	v_exp_f32_e32 v3, v3
	v_mul_f32_e32 v4, 0x3fb8aa3b, v4
	v_sub_f32_e32 v5, v53, v136
	v_add_f32_e32 v2, v2, v137
	v_exp_f32_e32 v4, v4
	v_mul_f32_e32 v5, 0x3fb8aa3b, v5
	v_sub_f32_e32 v137, v56, v136
	v_exp_f32_e32 v5, v5
	v_mul_f32_e32 v137, 0x3fb8aa3b, v137
	v_exp_f32_e32 v137, v137
	v_add_f32_e32 v2, v2, v3
	v_sub_f32_e32 v3, v35, v136
	v_add_f32_e32 v2, v2, v4
	v_mul_f32_e32 v3, 0x3fb8aa3b, v3
	v_sub_f32_e32 v4, v38, v136
	v_add_f32_e32 v2, v2, v5
	v_exp_f32_e32 v3, v3
	v_mul_f32_e32 v4, 0x3fb8aa3b, v4
	v_sub_f32_e32 v5, v42, v136
	v_add_f32_e32 v2, v2, v137
	v_exp_f32_e32 v4, v4
	v_mul_f32_e32 v5, 0x3fb8aa3b, v5
	v_sub_f32_e32 v137, v44, v136
	v_exp_f32_e32 v5, v5
	v_mul_f32_e32 v137, 0x3fb8aa3b, v137
	v_exp_f32_e32 v137, v137
	v_add_f32_e32 v2, v2, v3
	v_sub_f32_e32 v3, v39, v136
	v_add_f32_e32 v2, v2, v4
	v_mul_f32_e32 v3, 0x3fb8aa3b, v3
	v_sub_f32_e32 v4, v41, v136
	v_add_f32_e32 v2, v2, v5
	v_exp_f32_e32 v3, v3
	v_mul_f32_e32 v4, 0x3fb8aa3b, v4
	v_sub_f32_e32 v5, v45, v136
	v_add_f32_e32 v2, v2, v137
	v_exp_f32_e32 v4, v4
	v_mul_f32_e32 v5, 0x3fb8aa3b, v5
	v_sub_f32_e32 v137, v48, v136
	v_exp_f32_e32 v5, v5
	v_mul_f32_e32 v137, 0x3fb8aa3b, v137
	v_exp_f32_e32 v137, v137
	v_add_f32_e32 v2, v2, v3
	v_sub_f32_e32 v3, v27, v136
	v_add_f32_e32 v2, v2, v4
	v_mul_f32_e32 v3, 0x3fb8aa3b, v3
	v_sub_f32_e32 v4, v30, v136
	v_add_f32_e32 v2, v2, v5
	v_exp_f32_e32 v3, v3
	v_mul_f32_e32 v4, 0x3fb8aa3b, v4
	v_sub_f32_e32 v5, v34, v136
	v_add_f32_e32 v2, v2, v137
	v_exp_f32_e32 v4, v4
	v_mul_f32_e32 v5, 0x3fb8aa3b, v5
	v_sub_f32_e32 v137, v36, v136
	v_exp_f32_e32 v5, v5
	v_mul_f32_e32 v137, 0x3fb8aa3b, v137
	v_exp_f32_e32 v137, v137
	v_add_f32_e32 v2, v2, v3
	v_sub_f32_e32 v3, v31, v136
	v_add_f32_e32 v2, v2, v4
	v_mul_f32_e32 v3, 0x3fb8aa3b, v3
	v_sub_f32_e32 v4, v33, v136
	v_add_f32_e32 v2, v2, v5
	v_exp_f32_e32 v3, v3
	v_mul_f32_e32 v4, 0x3fb8aa3b, v4
	v_sub_f32_e32 v5, v37, v136
	v_add_f32_e32 v2, v2, v137
	v_exp_f32_e32 v4, v4
	v_mul_f32_e32 v5, 0x3fb8aa3b, v5
	v_sub_f32_e32 v137, v40, v136
	v_exp_f32_e32 v5, v5
	v_mul_f32_e32 v137, 0x3fb8aa3b, v137
	v_exp_f32_e32 v137, v137
	v_add_f32_e32 v2, v2, v3
	v_sub_f32_e32 v3, v22, v136
	v_add_f32_e32 v2, v2, v4
	v_mul_f32_e32 v3, 0x3fb8aa3b, v3
	v_sub_f32_e32 v4, v23, v136
	v_add_f32_e32 v2, v2, v5
	v_exp_f32_e32 v3, v3
	v_mul_f32_e32 v4, 0x3fb8aa3b, v4
	v_sub_f32_e32 v5, v26, v136
	v_add_f32_e32 v2, v2, v137
	v_exp_f32_e32 v4, v4
	v_mul_f32_e32 v5, 0x3fb8aa3b, v5
	v_sub_f32_e32 v137, v28, v136
	v_exp_f32_e32 v5, v5
	v_mul_f32_e32 v137, 0x3fb8aa3b, v137
	v_exp_f32_e32 v137, v137
	v_add_f32_e32 v2, v2, v3
	v_sub_f32_e32 v3, v24, v136
	v_add_f32_e32 v2, v2, v4
	v_mul_f32_e32 v3, 0x3fb8aa3b, v3
	v_sub_f32_e32 v4, v25, v136
	v_add_f32_e32 v2, v2, v5
	v_exp_f32_e32 v3, v3
	v_mul_f32_e32 v4, 0x3fb8aa3b, v4
	v_sub_f32_e32 v5, v29, v136
	v_add_f32_e32 v2, v2, v137
	v_exp_f32_e32 v4, v4
	v_mul_f32_e32 v5, 0x3fb8aa3b, v5
	v_sub_f32_e32 v137, v32, v136
	v_exp_f32_e32 v5, v5
	v_mul_f32_e32 v137, 0x3fb8aa3b, v137
	v_exp_f32_e32 v137, v137
	v_add_f32_e32 v2, v2, v3
	v_add_f32_e32 v2, v2, v4
	v_add_f32_e32 v2, v2, v5
	v_add_f32_e32 v2, v2, v137
	s_and_saveexec_b64 s[12:13], vcc
	s_cbranch_execnz .LBB2_28
	s_or_b64 exec, exec, s[12:13]
	s_and_saveexec_b64 s[12:13], s[2:3]
	s_cbranch_execnz .LBB2_29

.LBB2_23:
	s_or_b64 exec, exec, s[12:13]
	s_waitcnt lgkmcnt(1)
	v_mov_b32_e32 v136, 0
	s_waitcnt lgkmcnt(0)
	s_barrier
	ds_read_b128 v[2:5], v136
	ds_read_b128 v[136:139], v136 offset:16
	s_mov_b32 s12, 0x800000
	s_waitcnt lgkmcnt(1)
	v_max_f32_e32 v140, v5, v5
	v_max_f32_e32 v141, v4, v4
	v_max_f32_e32 v140, v141, v140
	v_max3_f32 v140, v2, v3, v140
	v_sub_f32_e32 v2, v2, v140
	v_sub_f32_e32 v3, v3, v140
	v_mul_f32_e32 v2, 0x3fb8aa3b, v2
	v_mul_f32_e32 v3, 0x3fb8aa3b, v3
	v_sub_f32_e32 v4, v4, v140
	v_sub_f32_e32 v5, v5, v140
	v_exp_f32_e32 v2, v2
	v_exp_f32_e32 v3, v3
	v_mul_f32_e32 v4, 0x3fb8aa3b, v4
	v_mul_f32_e32 v5, 0x3fb8aa3b, v5
	v_exp_f32_e32 v4, v4
	v_exp_f32_e32 v5, v5
	s_waitcnt lgkmcnt(0)
	v_pk_mul_f32 v[2:3], v[136:137], v[2:3]
	v_pk_mul_f32 v[4:5], v[138:139], v[4:5]
	v_add_f32_e32 v2, v2, v3
	v_add_f32_e32 v2, v4, v2
	v_add_f32_e32 v2, v5, v2
	v_cmp_gt_f32_e32 vcc, s12, v2
	s_and_b64 s[12:13], vcc, exec
	s_cselect_b32 s12, 32, 0
	v_ldexp_f32 v2, v2, s12
	v_log_f32_e32 v2, v2
	s_mov_b32 s12, 0x3f317217
	v_mov_b32_e32 v3, 0x41b17218
	v_cndmask_b32_e32 v3, 0, v3, vcc
	v_mul_f32_e32 v5, 0x3f317217, v2
	v_fma_f32 v5, v2, s12, -v5
	v_fmamk_f32 v5, v2, 0x3377d1cf, v5
	s_mov_b32 s12, 0x7f800000
	v_fmac_f32_e32 v5, 0x3f317217, v2
	v_cmp_lt_f32_e64 vcc, |v2|, s12
	s_lshl_b64 s[10:11], s[10:11], 2
	v_lshrrev_b32_e32 v143, 2, v0
	v_and_b32_e32 v142, 3, v0
	v_lshlrev_b32_e32 v143, 7, v143
	v_lshl_or_b32 v143, v142, 4, v143
	v_mov_b32_e32 v4, v143
	v_cndmask_b32_e32 v2, v2, v5, vcc
	v_sub_f32_e32 v2, v2, v3
	v_add_f32_e32 v2, v140, v2
	s_add_u32 s0, s0, s10
	s_addc_u32 s1, s1, s11
	v_sub_f32_e32 v139, v133, v2
	v_sub_f32_e32 v138, v132, v2
	v_sub_f32_e32 v137, v126, v2
	v_sub_f32_e32 v136, v124, v2
	v_sub_f32_e32 v127, v127, v2
	v_sub_f32_e32 v126, v125, v2
	v_sub_f32_e32 v125, v120, v2
	v_sub_f32_e32 v124, v117, v2
	v_or_b32_e32 v3, 0x2000, v4
	v_sub_f32_e32 v135, v135, v2
	v_sub_f32_e32 v134, v134, v2
	v_sub_f32_e32 v133, v131, v2
	v_sub_f32_e32 v132, v129, v2
	global_store_dwordx4 v4, v[136:139], s[0:1]
	global_store_dwordx4 v4, v[132:135], s[0:1] offset:64
	v_sub_f32_e32 v131, v130, v2
	v_sub_f32_e32 v130, v128, v2
	v_sub_f32_e32 v129, v123, v2
	v_sub_f32_e32 v128, v121, v2
	global_store_dwordx4 v3, v[124:127], s[0:1]
	global_store_dwordx4 v3, v[128:131], s[0:1] offset:64
	v_sub_f32_e32 v120, v119, v2
	v_sub_f32_e32 v127, v118, v2
	v_sub_f32_e32 v126, v116, v2
	v_sub_f32_e32 v125, v112, v2
	v_sub_f32_e32 v124, v109, v2
	v_sub_f32_e32 v119, v115, v2
	v_sub_f32_e32 v118, v113, v2
	v_or_b32_e32 v3, 0x4000, v4
	v_sub_f32_e32 v121, v122, v2
	global_store_dwordx4 v3, v[124:127], s[0:1]
	global_store_dwordx4 v3, v[118:121], s[0:1] offset:64
	v_sub_f32_e32 v117, v104, v2
	v_sub_f32_e32 v116, v101, v2
	v_sub_f32_e32 v119, v110, v2
	v_sub_f32_e32 v118, v108, v2
	v_sub_f32_e32 v112, v111, v2
	v_sub_f32_e32 v111, v107, v2
	v_sub_f32_e32 v110, v105, v2
	v_or_b32_e32 v3, 0x6000, v4
	v_sub_f32_e32 v113, v114, v2
	global_store_dwordx4 v3, v[116:119], s[0:1]
	global_store_dwordx4 v3, v[110:113], s[0:1] offset:64
	v_sub_f32_e32 v109, v96, v2
	v_sub_f32_e32 v108, v93, v2
	v_sub_f32_e32 v111, v102, v2
	v_sub_f32_e32 v110, v100, v2
	v_sub_f32_e32 v104, v103, v2
	v_sub_f32_e32 v103, v99, v2
	v_sub_f32_e32 v102, v97, v2
	v_or_b32_e32 v3, 0x8000, v4
	v_sub_f32_e32 v105, v106, v2
	global_store_dwordx4 v3, v[108:111], s[0:1]
	global_store_dwordx4 v3, v[102:105], s[0:1] offset:64
	v_sub_f32_e32 v101, v88, v2
	v_sub_f32_e32 v100, v85, v2
	v_sub_f32_e32 v103, v94, v2
	v_sub_f32_e32 v102, v92, v2
	v_sub_f32_e32 v96, v95, v2
	v_sub_f32_e32 v95, v91, v2
	v_sub_f32_e32 v94, v89, v2
	v_or_b32_e32 v3, 0xa000, v4
	v_sub_f32_e32 v97, v98, v2
	global_store_dwordx4 v3, v[100:103], s[0:1]
	global_store_dwordx4 v3, v[94:97], s[0:1] offset:64
	v_sub_f32_e32 v93, v72, v2
	v_sub_f32_e32 v92, v63, v2
	v_sub_f32_e32 v95, v86, v2
	v_sub_f32_e32 v94, v80, v2
	v_sub_f32_e32 v89, v90, v2
	v_sub_f32_e32 v88, v87, v2
	v_sub_f32_e32 v87, v79, v2
	v_sub_f32_e32 v86, v73, v2
	v_or_b32_e32 v3, 0xc000, v4
	global_store_dwordx4 v3, v[92:95], s[0:1]
	global_store_dwordx4 v3, v[86:89], s[0:1] offset:64
	v_or_b32_e32 v3, 0xe000, v4
	v_sub_f32_e32 v93, v74, v2
	v_sub_f32_e32 v89, v64, v2
	v_sub_f32_e32 v88, v60, v2
	v_sub_f32_e32 v87, v54, v2
	v_sub_f32_e32 v86, v51, v2
	v_sub_f32_e32 v92, v65, v2
	v_sub_f32_e32 v91, v57, v2
	v_sub_f32_e32 v90, v55, v2
	global_store_dwordx4 v3, v[86:89], s[0:1]
	global_store_dwordx4 v3, v[90:93], s[0:1] offset:64
	v_sub_f32_e32 v54, v53, v2
	v_sub_f32_e32 v89, v52, v2
	v_sub_f32_e32 v88, v50, v2
	v_sub_f32_e32 v87, v46, v2
	v_sub_f32_e32 v86, v43, v2
	v_sub_f32_e32 v53, v49, v2
	v_sub_f32_e32 v52, v47, v2
	v_or_b32_e32 v3, 0x10000, v4
	v_sub_f32_e32 v55, v56, v2
	global_store_dwordx4 v3, v[86:89], s[0:1]
	global_store_dwordx4 v3, v[52:55], s[0:1] offset:64
	v_sub_f32_e32 v51, v38, v2
	v_sub_f32_e32 v50, v35, v2
	v_sub_f32_e32 v53, v44, v2
	v_sub_f32_e32 v52, v42, v2
	v_sub_f32_e32 v46, v45, v2
	v_sub_f32_e32 v45, v41, v2
	v_sub_f32_e32 v44, v39, v2
	v_or_b32_e32 v3, 0x12000, v4
	v_sub_f32_e32 v47, v48, v2
	global_store_dwordx4 v3, v[50:53], s[0:1]
	global_store_dwordx4 v3, v[44:47], s[0:1] offset:64
	v_sub_f32_e32 v43, v30, v2
	v_sub_f32_e32 v42, v27, v2
	v_sub_f32_e32 v45, v36, v2
	v_sub_f32_e32 v44, v34, v2
	v_sub_f32_e32 v38, v37, v2
	v_sub_f32_e32 v37, v33, v2
	v_sub_f32_e32 v36, v31, v2
	v_or_b32_e32 v3, 0x14000, v4
	v_sub_f32_e32 v39, v40, v2
	global_store_dwordx4 v3, v[42:45], s[0:1]
	global_store_dwordx4 v3, v[36:39], s[0:1] offset:64
	v_sub_f32_e32 v35, v23, v2
	v_sub_f32_e32 v34, v22, v2
	v_sub_f32_e32 v37, v28, v2
	v_sub_f32_e32 v36, v26, v2
	v_or_b32_e32 v3, 0x16000, v4
	v_sub_f32_e32 v27, v32, v2
	v_sub_f32_e32 v26, v29, v2
	v_sub_f32_e32 v25, v25, v2
	v_sub_f32_e32 v24, v24, v2
	global_store_dwordx4 v3, v[34:37], s[0:1]
	global_store_dwordx4 v3, v[24:27], s[0:1] offset:64
	s_and_saveexec_b64 s[10:11], s[8:9]
	s_cbranch_execnz .LBB2_31
	s_or_b64 exec, exec, s[10:11]
	s_and_saveexec_b64 s[8:9], s[2:3]
	s_cbranch_execnz .LBB2_32

.LBB2_31:
	v_sub_f32_e32 v24, v20, v2
	v_sub_f32_e32 v22, v18, v2
	v_sub_f32_e32 v25, v19, v2
	v_sub_f32_e32 v23, v6, v2
	v_add_u32_e32 v1, 0x18000, v143
	v_sub_f32_e32 v20, v21, v2
	v_sub_f32_e32 v18, v15, v2
	v_sub_f32_e32 v21, v16, v2
	v_sub_f32_e32 v19, v14, v2
	global_store_dwordx4 v1, v[22:25], s[0:1]
	global_store_dwordx4 v1, v[18:21], s[0:1] offset:64
	s_or_b64 exec, exec, s[10:11]
	s_and_saveexec_b64 s[8:9], s[2:3]
	s_cbranch_execz .LBB2_25
.LBB2_32:
	v_mov_b32_e32 v1, 0x1a000
	v_sub_f32_e32 v20, v83, v2
	v_sub_f32_e32 v18, v77, v2
	v_sub_f32_e32 v21, v81, v2
	v_sub_f32_e32 v19, v75, v2
	v_or_b32_e32 v1, v1, v143
	v_sub_f32_e32 v24, v84, v2
	v_sub_f32_e32 v22, v78, v2
	v_sub_f32_e32 v25, v82, v2
	v_sub_f32_e32 v23, v76, v2
	global_store_dwordx4 v1, v[18:21], s[0:1]
	global_store_dwordx4 v1, v[22:25], s[0:1] offset:64
	s_or_b64 exec, exec, s[8:9]
	s_and_saveexec_b64 s[2:3], s[4:5]
	s_cbranch_execz .LBB2_26
.LBB2_33:
	v_mov_b32_e32 v1, 0x1c000
	v_sub_f32_e32 v20, v68, v2
	v_sub_f32_e32 v18, v61, v2
	v_sub_f32_e32 v21, v66, v2
	v_sub_f32_e32 v19, v58, v2
	v_or_b32_e32 v1, v1, v143
	v_sub_f32_e32 v24, v69, v2
	v_sub_f32_e32 v22, v62, v2
	v_sub_f32_e32 v25, v67, v2
	v_sub_f32_e32 v23, v59, v2
	global_store_dwordx4 v1, v[18:21], s[0:1]
	global_store_dwordx4 v1, v[22:25], s[0:1] offset:64
	s_or_b64 exec, exec, s[2:3]
	s_and_saveexec_b64 s[2:3], s[6:7]
	s_cbranch_execz .LBB2_27
.LBB2_34:
	v_mov_b32_e32 v1, 0x1e000
	v_sub_f32_e32 v20, v13, v2
	v_sub_f32_e32 v18, v9, v2
	v_sub_f32_e32 v21, v11, v2
	v_sub_f32_e32 v19, v7, v2
	v_or_b32_e32 v0, v1, v143
	v_sub_f32_e32 v6, v17, v2
	v_sub_f32_e32 v4, v10, v2
	v_sub_f32_e32 v7, v12, v2
	v_sub_f32_e32 v5, v8, v2
	global_store_dwordx4 v0, v[18:21], s[0:1]
	global_store_dwordx4 v0, v[4:7], s[0:1] offset:64
	s_endpgm
	s_nop 0
	s_nop 0
	s_nop 0
	s_nop 0
	s_nop 0
	s_nop 0
	s_nop 0
	s_nop 0
	s_nop 0
	s_nop 0
	s_nop 0
	s_nop 0
	s_nop 0
	s_nop 0
	s_nop 0
	s_nop 0
	s_nop 0
	s_nop 0
	s_nop 0
	s_nop 0
	s_nop 0
	s_nop 0
	s_nop 0
	s_nop 0
	s_nop 0
	s_nop 0
	s_nop 0
	s_nop 0
	s_nop 0
	s_nop 0
	s_nop 0
	s_nop 0
	s_nop 0
	s_nop 0
	s_nop 0
	s_nop 0
	s_nop 0
	s_nop 0
	s_nop 0
	s_nop 0
	s_nop 0
	s_nop 0
	s_nop 0
	s_nop 0
	s_nop 0
	s_nop 0
	s_nop 0
	s_endpgm

	.amdhsa_kernel _Z11k_lse_finalPKDF16_Pf
		.amdhsa_group_segment_fixed_size 32
		.amdhsa_private_segment_fixed_size 0
		.amdhsa_kernarg_size 16
		.amdhsa_user_sgpr_count 2
		.amdhsa_user_sgpr_dispatch_ptr 0
		.amdhsa_user_sgpr_queue_ptr 0
		.amdhsa_user_sgpr_kernarg_segment_ptr 1
		.amdhsa_user_sgpr_dispatch_id 0
		.amdhsa_user_sgpr_kernarg_preload_length 0
		.amdhsa_user_sgpr_kernarg_preload_offset 0
		.amdhsa_user_sgpr_private_segment_size 0
		.amdhsa_uses_dynamic_stack 0
		.amdhsa_enable_private_segment 0
		.amdhsa_system_sgpr_workgroup_id_x 1
		.amdhsa_system_sgpr_workgroup_id_y 0
		.amdhsa_system_sgpr_workgroup_id_z 0
		.amdhsa_system_sgpr_workgroup_info 0
		.amdhsa_system_vgpr_workitem_id 0
		.amdhsa_next_free_vgpr 148
		.amdhsa_next_free_sgpr 14
		.amdhsa_accum_offset 148
		.amdhsa_reserve_vcc 1
		.amdhsa_float_round_mode_32 0
		.amdhsa_float_round_mode_16_64 0
		.amdhsa_float_denorm_mode_32 3
		.amdhsa_float_denorm_mode_16_64 3
		.amdhsa_dx10_clamp 1
		.amdhsa_ieee_mode 1
		.amdhsa_fp16_overflow 0
		.amdhsa_tg_split 0
		.amdhsa_exception_fp_ieee_invalid_op 0
		.amdhsa_exception_fp_denorm_src 0
		.amdhsa_exception_fp_ieee_div_zero 0
		.amdhsa_exception_fp_ieee_overflow 0
		.amdhsa_exception_fp_ieee_underflow 0
		.amdhsa_exception_fp_ieee_inexact 0
		.amdhsa_exception_int_div_zero 0
	.end_amdhsa_kernel

amdhsa.kernels:
  - .agpr_count:     0
    .args:
      - .offset:         0
        .size:           200
        .value_kind:     by_value
    .group_segment_fixed_size: 4224
    .kernarg_segment_align: 8
    .kernarg_segment_size: 200
    .language:       OpenCL C
    .language_version:
      - 2
      - 0
    .max_flat_workgroup_size: 256
    .name:           _Z10k_prep_all8PrepArgs
    .private_segment_fixed_size: 0
    .sgpr_count:     74
    .sgpr_spill_count: 0
    .symbol:         _Z10k_prep_all8PrepArgs.kd
    .uniform_work_group_size: 1
    .uses_dynamic_stack: false
    .vgpr_count:     27
    .vgpr_spill_count: 0
    .wavefront_size: 64
  - .agpr_count:     0
    .args:
      - .offset:         0
        .size:           192
        .value_kind:     by_value
    .group_segment_fixed_size: 0
    .kernarg_segment_align: 8
    .kernarg_segment_size: 192
    .language:       OpenCL C
    .language_version:
      - 2
      - 0
    .max_flat_workgroup_size: 512
    .name:           _Z9k_persist11PersistArgs
    .private_segment_fixed_size: 0
    .sgpr_count:     106
    .sgpr_spill_count: 32
    .symbol:         _Z9k_persist11PersistArgs.kd
    .uniform_work_group_size: 1
    .uses_dynamic_stack: false
    .vgpr_count:     241
    .vgpr_spill_count: 0
    .wavefront_size: 64
  - .agpr_count:     0
    .args:
      - .actual_access:  read_only
        .address_space:  global
        .offset:         0
        .size:           8
        .value_kind:     global_buffer
      - .actual_access:  write_only
        .address_space:  global
        .offset:         8
        .size:           8
        .value_kind:     global_buffer
    .group_segment_fixed_size: 32
    .kernarg_segment_align: 8
    .kernarg_segment_size: 16
    .language:       OpenCL C
    .language_version:
      - 2
      - 0
    .max_flat_workgroup_size: 256
    .name:           _Z11k_lse_finalPKDF16_Pf
    .private_segment_fixed_size: 0
    .sgpr_count:     20
    .sgpr_spill_count: 0
    .symbol:         _Z11k_lse_finalPKDF16_Pf.kd
    .uniform_work_group_size: 1
    .uses_dynamic_stack: false
    .vgpr_count:     148
    .vgpr_spill_count: 0
    .wavefront_size: 64
  - .agpr_count:     0
    .args:
      - .address_space:  global
        .offset:         0
        .size:           8
        .value_kind:     global_buffer
      - .address_space:  global
        .offset:         8
        .size:           8
        .value_kind:     global_buffer
      - .actual_access:  write_only
        .address_space:  global
        .offset:         16
        .size:           8
        .value_kind:     global_buffer
      - .actual_access:  read_only
        .address_space:  global
        .offset:         24
        .size:           8
        .value_kind:     global_buffer
      - .actual_access:  read_only
        .address_space:  global
        .offset:         32
        .size:           8
        .value_kind:     global_buffer
      - .actual_access:  read_only
        .address_space:  global
        .offset:         40
        .size:           8
        .value_kind:     global_buffer
      - .offset:         48
        .size:           4
        .value_kind:     by_value
      - .offset:         52
        .size:           4
        .value_kind:     by_value
      - .actual_access:  read_only
        .address_space:  global
        .offset:         56
        .size:           8
        .value_kind:     global_buffer
      - .actual_access:  read_only
        .address_space:  global
        .offset:         64
        .size:           8
        .value_kind:     global_buffer
      - .actual_access:  read_only
        .address_space:  global
        .offset:         72
        .size:           8
        .value_kind:     global_buffer
    .group_segment_fixed_size: 0
    .kernarg_segment_align: 8
    .kernarg_segment_size: 80
    .language:       OpenCL C
    .language_version:
      - 2
      - 0
    .max_flat_workgroup_size: 512
    .name:           _Z6k_gemmILi8ELi512ELi0ELb0ELi0EEvPKDF16_S1_PfPDF16_S3_PKfiiS1_S1_S3_
    .private_segment_fixed_size: 0
    .sgpr_count:     32
    .sgpr_spill_count: 0
    .symbol:         _Z6k_gemmILi8ELi512ELi0ELb0ELi0EEvPKDF16_S1_PfPDF16_S3_PKfiiS1_S1_S3_.kd
    .uniform_work_group_size: 1
    .uses_dynamic_stack: false
    .vgpr_count:     246
    .vgpr_spill_count: 0
    .wavefront_size: 64
  - .agpr_count:     0
    .args:
      - .address_space:  global
        .offset:         0
        .size:           8
        .value_kind:     global_buffer
      - .address_space:  global
        .offset:         8
        .size:           8
        .value_kind:     global_buffer
      - .actual_access:  read_only
        .address_space:  global
        .offset:         16
        .size:           8
        .value_kind:     global_buffer
      - .actual_access:  write_only
        .address_space:  global
        .offset:         24
        .size:           8
        .value_kind:     global_buffer
      - .actual_access:  read_only
        .address_space:  global
        .offset:         32
        .size:           8
        .value_kind:     global_buffer
      - .actual_access:  read_only
        .address_space:  global
        .offset:         40
        .size:           8
        .value_kind:     global_buffer
      - .offset:         48
        .size:           4
        .value_kind:     by_value
      - .offset:         52
        .size:           4
        .value_kind:     by_value
      - .actual_access:  read_only
        .address_space:  global
        .offset:         56
        .size:           8
        .value_kind:     global_buffer
      - .actual_access:  read_only
        .address_space:  global
        .offset:         64
        .size:           8
        .value_kind:     global_buffer
      - .actual_access:  read_only
        .address_space:  global
        .offset:         72
        .size:           8
        .value_kind:     global_buffer
    .group_segment_fixed_size: 0
    .kernarg_segment_align: 8
    .kernarg_segment_size: 80
    .language:       OpenCL C
    .language_version:
      - 2
      - 0
    .max_flat_workgroup_size: 512
    .name:           _Z6k_gemmILi16ELi1024ELi0ELb0ELi3EEvPKDF16_S1_PfPDF16_S3_PKfiiS1_S1_S3_
    .private_segment_fixed_size: 0
    .sgpr_count:     36
    .sgpr_spill_count: 0
    .symbol:         _Z6k_gemmILi16ELi1024ELi0ELb0ELi3EEvPKDF16_S1_PfPDF16_S3_PKfiiS1_S1_S3_.kd
    .uniform_work_group_size: 1
    .uses_dynamic_stack: false
    .vgpr_count:     246
    .vgpr_spill_count: 0
    .wavefront_size: 64
  - .agpr_count:     0
    .args:
      - .address_space:  global
        .offset:         0
        .size:           8
        .value_kind:     global_buffer
      - .address_space:  global
        .offset:         8
        .size:           8
        .value_kind:     global_buffer
      - .actual_access:  read_only
        .address_space:  global
        .offset:         16
        .size:           8
        .value_kind:     global_buffer
      - .actual_access:  write_only
        .address_space:  global
        .offset:         24
        .size:           8
        .value_kind:     global_buffer
      - .actual_access:  write_only
        .address_space:  global
        .offset:         32
        .size:           8
        .value_kind:     global_buffer
      - .actual_access:  read_only
        .address_space:  global
        .offset:         40
        .size:           8
        .value_kind:     global_buffer
      - .offset:         48
        .size:           4
        .value_kind:     by_value
      - .offset:         52
        .size:           4
        .value_kind:     by_value
      - .address_space:  global
        .offset:         56
        .size:           8
        .value_kind:     global_buffer
      - .address_space:  global
        .offset:         64
        .size:           8
        .value_kind:     global_buffer
      - .actual_access:  write_only
        .address_space:  global
        .offset:         72
        .size:           8
        .value_kind:     global_buffer
    .group_segment_fixed_size: 0
    .kernarg_segment_align: 8
    .kernarg_segment_size: 80
    .language:       OpenCL C
    .language_version:
      - 2
      - 0
    .max_flat_workgroup_size: 512
    .name:           _Z6k_gemmILi48ELi2048ELi1ELb1ELi12EEvPKDF16_S1_PfPDF16_S3_PKfiiS1_S1_S3_
    .private_segment_fixed_size: 0
    .sgpr_count:     26
    .sgpr_spill_count: 0
    .symbol:         _Z6k_gemmILi48ELi2048ELi1ELb1ELi12EEvPKDF16_S1_PfPDF16_S3_PKfiiS1_S1_S3_.kd
    .uniform_work_group_size: 1
    .uses_dynamic_stack: false
    .vgpr_count:     242
    .vgpr_spill_count: 0
    .wavefront_size: 64
